# instruction selection: per-unit GEMM accumulator zeroing (20 runs of ~127 v_mov_b32 from a zero register) done with v_mov_b64 pairs (1235 fewer VALU issues per pass over the runs); on top of v59
# baseline (speedup 1.0000x reference)
.LBB0_449:
	s_lshl_b32 s43, s42, 20
	s_lshl_b32 s44, s41, 20
	s_and_b64 vcc, exec, s[0:1]
	v_mov_b32_e32 v125, 0
	s_cbranch_vccnz .LBB0_445
	v_cmp_lt_i64_e32 vcc, s[14:15], v[130:131]
	s_and_b64 s[14:15], vcc, exec
	v_mov_b32_e32 v2, 0
	s_cselect_b32 s14, s43, s45
	s_cselect_b32 s15, s44, s46
	s_addk_i32 s45, 0x80
	s_addk_i32 s46, 0x100
	s_mov_b32 s47, 0
	s_nop 1
	v_mov_b32_e32 v3, 0
	v_mov_b64_e32 v[4:5], 0
	v_mov_b64_e32 v[6:7], 0
	v_mov_b64_e32 v[8:9], 0
	v_mov_b64_e32 v[10:11], 0
	v_mov_b64_e32 v[12:13], 0
	v_mov_b64_e32 v[14:15], 0
	v_mov_b64_e32 v[16:17], 0
	v_mov_b64_e32 v[18:19], 0
	v_mov_b64_e32 v[20:21], 0
	v_mov_b64_e32 v[22:23], 0
	v_mov_b64_e32 v[24:25], 0
	v_mov_b64_e32 v[26:27], 0
	v_mov_b64_e32 v[28:29], 0
	v_mov_b64_e32 v[30:31], 0
	v_mov_b64_e32 v[32:33], 0
	v_mov_b64_e32 v[34:35], 0
	v_mov_b64_e32 v[36:37], 0
	v_mov_b64_e32 v[38:39], 0
	v_mov_b64_e32 v[40:41], 0
	v_mov_b64_e32 v[42:43], 0
	v_mov_b64_e32 v[44:45], 0
	v_mov_b64_e32 v[46:47], 0
	v_mov_b64_e32 v[48:49], 0
	v_mov_b64_e32 v[50:51], 0
	v_mov_b64_e32 v[52:53], 0
	v_mov_b64_e32 v[54:55], 0
	v_mov_b64_e32 v[56:57], 0
	v_mov_b64_e32 v[58:59], 0
	v_mov_b64_e32 v[60:61], 0
	v_mov_b64_e32 v[62:63], 0
	v_mov_b64_e32 v[64:65], 0
	v_mov_b64_e32 v[66:67], 0
	v_mov_b64_e32 v[68:69], 0
	v_mov_b64_e32 v[70:71], 0
	v_mov_b64_e32 v[72:73], 0
	v_mov_b64_e32 v[74:75], 0
	v_mov_b64_e32 v[76:77], 0
	v_mov_b64_e32 v[78:79], 0
	v_mov_b64_e32 v[80:81], 0
	v_mov_b64_e32 v[82:83], 0
	v_mov_b64_e32 v[84:85], 0
	v_mov_b64_e32 v[86:87], 0
	v_mov_b64_e32 v[88:89], 0
	v_mov_b64_e32 v[90:91], 0
	v_mov_b64_e32 v[92:93], 0
	v_mov_b64_e32 v[94:95], 0
	v_mov_b64_e32 v[96:97], 0
	v_mov_b64_e32 v[98:99], 0
	v_mov_b64_e32 v[100:101], 0
	v_mov_b64_e32 v[102:103], 0
	v_mov_b64_e32 v[104:105], 0
	v_mov_b64_e32 v[106:107], 0
	v_mov_b64_e32 v[108:109], 0
	v_mov_b64_e32 v[110:111], 0
	v_mov_b64_e32 v[112:113], 0
	v_mov_b64_e32 v[114:115], 0
	v_mov_b64_e32 v[116:117], 0
	v_mov_b64_e32 v[118:119], 0
	v_mov_b64_e32 v[120:121], 0
	v_mov_b64_e32 v[122:123], 0
	v_mov_b64_e32 v[124:125], 0
	v_mov_b64_e32 v[126:127], 0
	v_mov_b64_e32 v[128:129], 0



.LBB0_462:
	s_lshl_b32 s39, s38, 19
	s_lshl_b32 s40, s37, 19
	s_and_b64 vcc, exec, s[0:1]
	v_mov_b32_e32 v129, 0
	s_cbranch_vccnz .LBB0_465
	v_mov_b64_e32 v[2:3], 0x280
	v_cmp_lt_i64_e32 vcc, s[16:17], v[2:3]
	s_and_b64 s[16:17], vcc, exec
	v_mov_b32_e32 v2, 0
	v_mov_b64_e32 v[252:253], 0x27f
	s_cselect_b32 s16, s39, s43
	s_cselect_b32 s17, s40, s44
	s_addk_i32 s43, 0x80
	s_addk_i32 s44, 0x100
	s_mov_b32 s45, 0
	s_nop 1
	v_mov_b32_e32 v3, 0
	v_mov_b64_e32 v[4:5], 0
	v_mov_b64_e32 v[6:7], 0
	v_mov_b64_e32 v[8:9], 0
	v_mov_b64_e32 v[10:11], 0
	v_mov_b64_e32 v[12:13], 0
	v_mov_b64_e32 v[14:15], 0
	v_mov_b64_e32 v[16:17], 0
	v_mov_b64_e32 v[18:19], 0
	v_mov_b64_e32 v[20:21], 0
	v_mov_b64_e32 v[22:23], 0
	v_mov_b64_e32 v[24:25], 0
	v_mov_b64_e32 v[26:27], 0
	v_mov_b64_e32 v[28:29], 0
	v_mov_b64_e32 v[30:31], 0
	v_mov_b64_e32 v[32:33], 0
	v_mov_b64_e32 v[34:35], 0
	v_mov_b64_e32 v[36:37], 0
	v_mov_b64_e32 v[38:39], 0
	v_mov_b64_e32 v[40:41], 0
	v_mov_b64_e32 v[42:43], 0
	v_mov_b64_e32 v[44:45], 0
	v_mov_b64_e32 v[46:47], 0
	v_mov_b64_e32 v[48:49], 0
	v_mov_b64_e32 v[50:51], 0
	v_mov_b64_e32 v[52:53], 0
	v_mov_b64_e32 v[54:55], 0
	v_mov_b64_e32 v[56:57], 0
	v_mov_b64_e32 v[58:59], 0
	v_mov_b64_e32 v[60:61], 0
	v_mov_b64_e32 v[62:63], 0
	v_mov_b64_e32 v[64:65], 0
	v_mov_b64_e32 v[70:71], 0
	v_mov_b64_e32 v[72:73], 0
	v_mov_b64_e32 v[74:75], 0
	v_mov_b64_e32 v[76:77], 0
	v_mov_b64_e32 v[78:79], 0
	v_mov_b64_e32 v[80:81], 0
	v_mov_b64_e32 v[82:83], 0
	v_mov_b64_e32 v[84:85], 0
	v_mov_b64_e32 v[86:87], 0
	v_mov_b64_e32 v[88:89], 0
	v_mov_b64_e32 v[90:91], 0
	v_mov_b64_e32 v[92:93], 0
	v_mov_b64_e32 v[94:95], 0
	v_mov_b64_e32 v[96:97], 0
	v_mov_b64_e32 v[98:99], 0
	v_mov_b64_e32 v[100:101], 0
	v_mov_b64_e32 v[102:103], 0
	v_mov_b64_e32 v[104:105], 0
	v_mov_b64_e32 v[106:107], 0
	v_mov_b64_e32 v[108:109], 0
	v_mov_b64_e32 v[110:111], 0
	v_mov_b64_e32 v[112:113], 0
	v_mov_b64_e32 v[114:115], 0
	v_mov_b64_e32 v[116:117], 0
	v_mov_b64_e32 v[118:119], 0
	v_mov_b64_e32 v[120:121], 0
	v_mov_b64_e32 v[122:123], 0
	v_mov_b64_e32 v[124:125], 0
	v_mov_b64_e32 v[126:127], 0
	v_mov_b64_e32 v[128:129], 0
	v_mov_b64_e32 v[232:233], 0
	v_mov_b64_e32 v[234:235], 0



.LBB0_618:
	s_mul_i32 s45, s44, 0x220000
	s_lshl_b32 s46, s43, 18
	s_and_b64 vcc, exec, s[0:1]
	v_mov_b32_e32 v125, 0
	s_cbranch_vccnz .LBB0_614
	v_cmp_lt_i64_e32 vcc, s[16:17], v[134:135]
	s_and_b64 s[16:17], vcc, exec
	v_mov_b32_e32 v2, 0
	s_cselect_b32 s16, s45, s47
	s_cselect_b32 s17, s46, s48
	s_addk_i32 s47, 0x80
	s_addk_i32 s48, 0x100
	s_mov_b32 s49, 0
	s_nop 1
	v_mov_b32_e32 v3, 0
	v_mov_b64_e32 v[4:5], 0
	v_mov_b64_e32 v[6:7], 0
	v_mov_b64_e32 v[8:9], 0
	v_mov_b64_e32 v[10:11], 0
	v_mov_b64_e32 v[12:13], 0
	v_mov_b64_e32 v[14:15], 0
	v_mov_b64_e32 v[16:17], 0
	v_mov_b64_e32 v[18:19], 0
	v_mov_b64_e32 v[20:21], 0
	v_mov_b64_e32 v[22:23], 0
	v_mov_b64_e32 v[24:25], 0
	v_mov_b64_e32 v[26:27], 0
	v_mov_b64_e32 v[28:29], 0
	v_mov_b64_e32 v[30:31], 0
	v_mov_b64_e32 v[32:33], 0
	v_mov_b64_e32 v[34:35], 0
	v_mov_b64_e32 v[36:37], 0
	v_mov_b64_e32 v[38:39], 0
	v_mov_b64_e32 v[40:41], 0
	v_mov_b64_e32 v[42:43], 0
	v_mov_b64_e32 v[44:45], 0
	v_mov_b64_e32 v[46:47], 0
	v_mov_b64_e32 v[48:49], 0
	v_mov_b64_e32 v[50:51], 0
	v_mov_b64_e32 v[52:53], 0
	v_mov_b64_e32 v[54:55], 0
	v_mov_b64_e32 v[56:57], 0
	v_mov_b64_e32 v[58:59], 0
	v_mov_b64_e32 v[60:61], 0
	v_mov_b64_e32 v[62:63], 0
	v_mov_b64_e32 v[64:65], 0
	v_mov_b64_e32 v[66:67], 0
	v_mov_b64_e32 v[68:69], 0
	v_mov_b64_e32 v[70:71], 0
	v_mov_b64_e32 v[72:73], 0
	v_mov_b64_e32 v[74:75], 0
	v_mov_b64_e32 v[76:77], 0
	v_mov_b64_e32 v[78:79], 0
	v_mov_b64_e32 v[80:81], 0
	v_mov_b64_e32 v[82:83], 0
	v_mov_b64_e32 v[84:85], 0
	v_mov_b64_e32 v[86:87], 0
	v_mov_b64_e32 v[88:89], 0
	v_mov_b64_e32 v[90:91], 0
	v_mov_b64_e32 v[92:93], 0
	v_mov_b64_e32 v[94:95], 0
	v_mov_b64_e32 v[96:97], 0
	v_mov_b64_e32 v[98:99], 0
	v_mov_b64_e32 v[100:101], 0
	v_mov_b64_e32 v[102:103], 0
	v_mov_b64_e32 v[104:105], 0
	v_mov_b64_e32 v[106:107], 0
	v_mov_b64_e32 v[108:109], 0
	v_mov_b64_e32 v[110:111], 0
	v_mov_b64_e32 v[112:113], 0
	v_mov_b64_e32 v[114:115], 0
	v_mov_b64_e32 v[116:117], 0
	v_mov_b64_e32 v[118:119], 0
	v_mov_b64_e32 v[120:121], 0
	v_mov_b64_e32 v[122:123], 0
	v_mov_b64_e32 v[124:125], 0
	v_mov_b64_e32 v[126:127], 0
	v_mov_b64_e32 v[128:129], 0



.LBB0_636:
	v_cmp_lt_i64_e64 s[2:3], s[2:3], v[134:135]
	s_mul_i32 s44, s43, 0x220000
	s_lshl_b32 s45, s42, 17
	s_andn2_b64 vcc, exec, s[22:23]
	v_mov_b32_e32 v129, 0
	s_cbranch_vccnz .LBB0_628
	s_and_b64 s[2:3], s[2:3], exec
	v_mov_b32_e32 v2, 0
	s_cselect_b32 s2, s44, s47
	s_cselect_b32 s3, s45, s7
	s_add_i32 s4, s47, 0x80
	s_add_i32 s5, s7, 0x100
	s_mov_b32 s7, 0
	s_nop 1
	v_mov_b32_e32 v3, 0
	v_mov_b64_e32 v[4:5], 0
	v_mov_b64_e32 v[6:7], 0
	v_mov_b64_e32 v[8:9], 0
	v_mov_b64_e32 v[10:11], 0
	v_mov_b64_e32 v[12:13], 0
	v_mov_b64_e32 v[14:15], 0
	v_mov_b64_e32 v[16:17], 0
	v_mov_b64_e32 v[18:19], 0
	v_mov_b64_e32 v[20:21], 0
	v_mov_b64_e32 v[22:23], 0
	v_mov_b64_e32 v[24:25], 0
	v_mov_b64_e32 v[26:27], 0
	v_mov_b64_e32 v[28:29], 0
	v_mov_b64_e32 v[30:31], 0
	v_mov_b64_e32 v[32:33], 0
	v_mov_b64_e32 v[34:35], 0
	v_mov_b64_e32 v[36:37], 0
	v_mov_b64_e32 v[38:39], 0
	v_mov_b64_e32 v[40:41], 0
	v_mov_b64_e32 v[42:43], 0
	v_mov_b64_e32 v[44:45], 0
	v_mov_b64_e32 v[46:47], 0
	v_mov_b64_e32 v[48:49], 0
	v_mov_b64_e32 v[50:51], 0
	v_mov_b64_e32 v[52:53], 0
	v_mov_b64_e32 v[54:55], 0
	v_mov_b64_e32 v[56:57], 0
	v_mov_b64_e32 v[58:59], 0
	v_mov_b64_e32 v[60:61], 0
	v_mov_b64_e32 v[62:63], 0
	v_mov_b64_e32 v[64:65], 0
	v_mov_b64_e32 v[66:67], 0
	v_mov_b64_e32 v[68:69], 0
	v_mov_b64_e32 v[70:71], 0
	v_mov_b64_e32 v[72:73], 0
	v_mov_b64_e32 v[74:75], 0
	v_mov_b64_e32 v[76:77], 0
	v_mov_b64_e32 v[78:79], 0
	v_mov_b64_e32 v[80:81], 0
	v_mov_b64_e32 v[82:83], 0
	v_mov_b64_e32 v[84:85], 0
	v_mov_b64_e32 v[86:87], 0
	v_mov_b64_e32 v[88:89], 0
	v_mov_b64_e32 v[90:91], 0
	v_mov_b64_e32 v[92:93], 0
	v_mov_b64_e32 v[94:95], 0
	v_mov_b64_e32 v[96:97], 0
	v_mov_b64_e32 v[98:99], 0
	v_mov_b64_e32 v[100:101], 0
	v_mov_b64_e32 v[102:103], 0
	v_mov_b64_e32 v[104:105], 0
	v_mov_b64_e32 v[106:107], 0
	v_mov_b64_e32 v[108:109], 0
	v_mov_b64_e32 v[110:111], 0
	v_mov_b64_e32 v[112:113], 0
	v_mov_b64_e32 v[114:115], 0
	v_mov_b64_e32 v[116:117], 0
	v_mov_b64_e32 v[118:119], 0
	v_mov_b64_e32 v[120:121], 0
	v_mov_b64_e32 v[122:123], 0
	v_mov_b64_e32 v[124:125], 0
	v_mov_b64_e32 v[126:127], 0
	v_mov_b64_e32 v[128:129], 0



.LBB0_1152:
	s_mul_i32 s39, s38, 0x30000
	s_mul_i32 s40, s37, 0x30000
	s_cmp_gt_i32 s37, 7
	s_cselect_b32 s43, 0x100, 0
	s_add_i32 s39, s39, s43
	s_add_i32 s40, s40, s43
	s_and_b64 vcc, exec, s[0:1]
	v_mov_b32_e32 v125, 0
	s_cbranch_vccnz .LBB0_1148
	v_cmp_lt_i64_e32 vcc, s[10:11], v[130:131]
	s_and_b64 s[10:11], vcc, exec
	v_mov_b32_e32 v2, 0
	s_cselect_b32 s10, s39, s41
	s_cselect_b32 s11, s40, s42
	s_addk_i32 s41, 0x80
	s_addk_i32 s42, 0x100
	s_mov_b32 s43, 0
	s_nop 1
	v_mov_b32_e32 v3, 0
	v_mov_b64_e32 v[4:5], 0
	v_mov_b64_e32 v[6:7], 0
	v_mov_b64_e32 v[8:9], 0
	v_mov_b64_e32 v[10:11], 0
	v_mov_b64_e32 v[12:13], 0
	v_mov_b64_e32 v[14:15], 0
	v_mov_b64_e32 v[16:17], 0
	v_mov_b64_e32 v[18:19], 0
	v_mov_b64_e32 v[20:21], 0
	v_mov_b64_e32 v[22:23], 0
	v_mov_b64_e32 v[24:25], 0
	v_mov_b64_e32 v[26:27], 0
	v_mov_b64_e32 v[28:29], 0
	v_mov_b64_e32 v[30:31], 0
	v_mov_b64_e32 v[32:33], 0
	v_mov_b64_e32 v[34:35], 0
	v_mov_b64_e32 v[36:37], 0
	v_mov_b64_e32 v[38:39], 0
	v_mov_b64_e32 v[40:41], 0
	v_mov_b64_e32 v[42:43], 0
	v_mov_b64_e32 v[44:45], 0
	v_mov_b64_e32 v[46:47], 0
	v_mov_b64_e32 v[48:49], 0
	v_mov_b64_e32 v[50:51], 0
	v_mov_b64_e32 v[52:53], 0
	v_mov_b64_e32 v[54:55], 0
	v_mov_b64_e32 v[56:57], 0
	v_mov_b64_e32 v[58:59], 0
	v_mov_b64_e32 v[60:61], 0
	v_mov_b64_e32 v[62:63], 0
	v_mov_b64_e32 v[64:65], 0
	v_mov_b64_e32 v[66:67], 0
	v_mov_b64_e32 v[68:69], 0
	v_mov_b64_e32 v[70:71], 0
	v_mov_b64_e32 v[72:73], 0
	v_mov_b64_e32 v[74:75], 0
	v_mov_b64_e32 v[76:77], 0
	v_mov_b64_e32 v[78:79], 0
	v_mov_b64_e32 v[80:81], 0
	v_mov_b64_e32 v[82:83], 0
	v_mov_b64_e32 v[84:85], 0
	v_mov_b64_e32 v[86:87], 0
	v_mov_b64_e32 v[88:89], 0
	v_mov_b64_e32 v[90:91], 0
	v_mov_b64_e32 v[92:93], 0
	v_mov_b64_e32 v[94:95], 0
	v_mov_b64_e32 v[96:97], 0
	v_mov_b64_e32 v[98:99], 0
	v_mov_b64_e32 v[100:101], 0
	v_mov_b64_e32 v[102:103], 0
	v_mov_b64_e32 v[104:105], 0
	v_mov_b64_e32 v[106:107], 0
	v_mov_b64_e32 v[108:109], 0
	v_mov_b64_e32 v[110:111], 0
	v_mov_b64_e32 v[112:113], 0
	v_mov_b64_e32 v[114:115], 0
	v_mov_b64_e32 v[116:117], 0
	v_mov_b64_e32 v[118:119], 0
	v_mov_b64_e32 v[120:121], 0
	v_mov_b64_e32 v[122:123], 0
	v_mov_b64_e32 v[124:125], 0
	v_mov_b64_e32 v[126:127], 0
	v_mov_b64_e32 v[128:129], 0



.LBB0_1288:
	v_mov_b32_e32 v2, v1
	s_ashr_i32 s24, s30, 6
	v_ashrrev_i32_e32 v5, 2, v2
	v_and_b32_e32 v4, -4, v5
	v_and_b32_e32 v6, 15, v2
	v_cmp_eq_u32_e32 vcc, v4, v6
	v_or_b32_e32 v3, 1, v4
	v_or_b32_e32 v4, 2, v4
	v_cndmask_b32_e64 v2, 0, 1.0, vcc
	v_cmp_eq_u32_e32 vcc, v3, v6
	s_and_b32 s0, s37, 48
	s_ashr_i32 s25, s24, 31
	v_cndmask_b32_e64 v3, 0, 1.0, vcc
	v_cmp_eq_u32_e32 vcc, v4, v6
	v_or_b32_e32 v5, 3, v5
	s_lshl_b32 s3, s30, 6
	s_lshl_b32 s2, s0, 9
	s_lshl_b64 s[0:1], s[24:25], 8
	v_cndmask_b32_e64 v4, 0, 1.0, vcc
	v_cmp_eq_u32_e32 vcc, v5, v6
	s_and_b32 s6, s3, 0x3c0
	s_add_u32 s41, s2, s0
	v_cndmask_b32_e64 v5, 0, 1.0, vcc
	s_addc_u32 s42, 0, s1
	s_mov_b64 s[26:27], 0
	s_nop 1
	v_mov_b64_e32 v[6:7], 0
	v_mov_b64_e32 v[8:9], 0
	v_mov_b64_e32 v[10:11], 0
	v_mov_b64_e32 v[12:13], 0
	v_mov_b64_e32 v[14:15], 0
	v_mov_b64_e32 v[16:17], 0
	v_mov_b64_e32 v[18:19], 0
	v_mov_b64_e32 v[20:21], 0
	v_mov_b64_e32 v[22:23], 0
	v_mov_b64_e32 v[24:25], 0
	v_mov_b64_e32 v[26:27], 0
	v_mov_b64_e32 v[28:29], 0
	v_mov_b64_e32 v[30:31], 0
	v_mov_b64_e32 v[32:33], 0
	v_mov_b64_e32 v[34:35], 0
	v_mov_b64_e32 v[36:37], 0
	v_mov_b64_e32 v[38:39], 0
	v_mov_b64_e32 v[40:41], 0
	v_mov_b64_e32 v[42:43], 0
	v_mov_b64_e32 v[44:45], 0
	v_mov_b64_e32 v[46:47], 0
	v_mov_b64_e32 v[48:49], 0
	v_mov_b64_e32 v[50:51], 0
	v_mov_b64_e32 v[52:53], 0
	v_mov_b64_e32 v[54:55], 0
	v_mov_b64_e32 v[56:57], 0
	v_mov_b64_e32 v[58:59], 0
	v_mov_b64_e32 v[60:61], 0
	v_mov_b64_e32 v[62:63], 0
	v_mov_b64_e32 v[64:65], 0
	v_mov_b64_e32 v[70:71], 0
	v_mov_b64_e32 v[72:73], 0
	v_mov_b64_e32 v[90:91], 0
	v_mov_b64_e32 v[92:93], 0
	v_mov_b64_e32 v[110:111], 0
	v_mov_b64_e32 v[112:113], 0
	v_mov_b64_e32 v[114:115], 0
	v_mov_b64_e32 v[116:117], 0
	v_mov_b64_e32 v[126:127], 0
	v_mov_b64_e32 v[128:129], 0


	v_mov_b32_e32 v74, v2
	v_mov_b32_e32 v75, v3
	v_mov_b32_e32 v76, v4
	v_mov_b32_e32 v77, v5
	v_mov_b32_e32 v94, v145
	v_mov_b32_e32 v95, v145
	v_mov_b32_e32 v96, v145
	v_mov_b32_e32 v97, v145
	v_mov_b32_e32 v98, v145
	v_mov_b32_e32 v99, v145
	v_mov_b32_e32 v100, v145
	v_mov_b32_e32 v101, v145
	v_mov_b32_e32 v66, v145
	v_mov_b32_e32 v67, v145
	v_mov_b32_e32 v68, v145
	v_mov_b32_e32 v69, v145
	v_mov_b32_e32 v82, v145
	v_mov_b32_e32 v83, v145
	v_mov_b32_e32 v84, v145
	v_mov_b32_e32 v85, v145
	v_mov_b32_e32 v102, v2
	v_mov_b32_e32 v103, v3
	v_mov_b32_e32 v104, v4
	v_mov_b32_e32 v105, v5
	v_mov_b32_e32 v118, v145
	v_mov_b32_e32 v119, v145
	v_mov_b32_e32 v120, v145
	v_mov_b32_e32 v121, v145
	v_mov_b32_e32 v78, v145
	v_mov_b32_e32 v79, v145
	v_mov_b32_e32 v80, v145
	v_mov_b32_e32 v81, v145
	v_mov_b32_e32 v86, v145
	v_mov_b32_e32 v87, v145
	v_mov_b32_e32 v88, v145
	v_mov_b32_e32 v89, v145
	v_mov_b32_e32 v106, v145
	v_mov_b32_e32 v107, v145
	v_mov_b32_e32 v108, v145
	v_mov_b32_e32 v109, v145
	v_mov_b32_e32 v122, v2
	v_mov_b32_e32 v123, v3
	v_mov_b32_e32 v124, v4
	v_mov_b32_e32 v125, v5
	s_branch .LBB0_1290

.LBB0_1520:
	v_cmp_lt_i64_e64 s[4:5], s[4:5], v[220:221]
	s_lshl_b32 s48, s29, 19
	s_lshl_b32 s49, s28, 19
	s_and_b64 vcc, exec, s[0:1]
	v_mov_b32_e32 v121, 0
	s_cbranch_vccnz .LBB0_1512
	s_and_b64 s[4:5], s[4:5], exec
	v_mov_b32_e32 v2, 0
	v_mov_b64_e32 v[252:253], 0x3ff
	s_cselect_b32 s4, s48, s52
	s_cselect_b32 s5, s49, s53
	s_addk_i32 s52, 0x80
	s_addk_i32 s53, 0x100
	s_mov_b32 s54, 0
	s_nop 1
	v_mov_b32_e32 v3, 0
	v_mov_b64_e32 v[4:5], 0
	v_mov_b64_e32 v[6:7], 0
	v_mov_b64_e32 v[8:9], 0
	v_mov_b64_e32 v[10:11], 0
	v_mov_b64_e32 v[12:13], 0
	v_mov_b64_e32 v[14:15], 0
	v_mov_b64_e32 v[16:17], 0
	v_mov_b64_e32 v[18:19], 0
	v_mov_b64_e32 v[20:21], 0
	v_mov_b64_e32 v[22:23], 0
	v_mov_b64_e32 v[24:25], 0
	v_mov_b64_e32 v[26:27], 0
	v_mov_b64_e32 v[28:29], 0
	v_mov_b64_e32 v[30:31], 0
	v_mov_b64_e32 v[32:33], 0
	v_mov_b64_e32 v[34:35], 0
	v_mov_b64_e32 v[36:37], 0
	v_mov_b64_e32 v[38:39], 0
	v_mov_b64_e32 v[40:41], 0
	v_mov_b64_e32 v[42:43], 0
	v_mov_b64_e32 v[44:45], 0
	v_mov_b64_e32 v[46:47], 0
	v_mov_b64_e32 v[48:49], 0
	v_mov_b64_e32 v[50:51], 0
	v_mov_b64_e32 v[52:53], 0
	v_mov_b64_e32 v[54:55], 0
	v_mov_b64_e32 v[56:57], 0
	v_mov_b64_e32 v[58:59], 0
	v_mov_b64_e32 v[60:61], 0
	v_mov_b64_e32 v[62:63], 0
	v_mov_b64_e32 v[64:65], 0
	v_mov_b64_e32 v[70:71], 0
	v_mov_b64_e32 v[72:73], 0
	v_mov_b64_e32 v[74:75], 0
	v_mov_b64_e32 v[76:77], 0
	v_mov_b64_e32 v[78:79], 0
	v_mov_b64_e32 v[80:81], 0
	v_mov_b64_e32 v[82:83], 0
	v_mov_b64_e32 v[84:85], 0
	v_mov_b64_e32 v[86:87], 0
	v_mov_b64_e32 v[88:89], 0
	v_mov_b64_e32 v[90:91], 0
	v_mov_b64_e32 v[92:93], 0
	v_mov_b64_e32 v[94:95], 0
	v_mov_b64_e32 v[96:97], 0
	v_mov_b64_e32 v[98:99], 0
	v_mov_b64_e32 v[100:101], 0
	v_mov_b64_e32 v[102:103], 0
	v_mov_b64_e32 v[104:105], 0
	v_mov_b64_e32 v[106:107], 0
	v_mov_b64_e32 v[108:109], 0
	v_mov_b64_e32 v[110:111], 0
	v_mov_b64_e32 v[112:113], 0
	v_mov_b64_e32 v[114:115], 0
	v_mov_b64_e32 v[116:117], 0
	v_mov_b64_e32 v[118:119], 0
	v_mov_b64_e32 v[120:121], 0
	v_mov_b64_e32 v[122:123], 0
	v_mov_b64_e32 v[124:125], 0
	v_mov_b64_e32 v[126:127], 0
	v_mov_b64_e32 v[128:129], 0
	v_mov_b64_e32 v[232:233], 0
	v_mov_b64_e32 v[234:235], 0



.LBB0_1838:
	s_lshl_b32 s69, s62, 19
	s_lshl_b32 s0, s61, 21
	s_add_i32 s69, s69, s0
	s_andn2_b64 vcc, exec, s[24:25]
	v_mov_b32_e32 v173, 0
	s_cbranch_vccnz .LBB0_1829
	v_add_u32_e32 v2, s66, v1
	v_cmp_le_i32_e32 vcc, s63, v2
	v_cmp_le_i32_e64 s[4:5], s65, v2
	v_mov_b32_e32 v6, s65
	v_cndmask_b32_e64 v3, 0, 1, vcc
	v_cndmask_b32_e64 v4, 0, 1, s[4:5]
	v_cmp_le_i32_e64 s[4:5], s64, v2
	v_mov_b32_e32 v7, s64
	v_cmp_gt_i32_e64 s[2:3], s67, v2
	v_addc_co_u32_e64 v3, s[4:5], v4, v3, s[4:5]
	v_mov_b32_e32 v4, s63
	v_cndmask_b32_e32 v5, 0, v4, vcc
	v_cmp_gt_i32_e32 vcc, s65, v2
	v_lshlrev_b32_e32 v197, 24, v3
	s_and_b64 s[0:1], s[28:29], exec
	v_cndmask_b32_e32 v5, v6, v5, vcc
	v_cmp_gt_i32_e32 vcc, s64, v2
	s_cselect_b32 s71, s69, s70
	s_cmp_eq_u32 s61, 64
	v_cndmask_b32_e32 v5, v7, v5, vcc
	v_sub_u32_e32 v196, v2, v5
	v_add_u32_e32 v2, s66, v178
	v_cmp_le_i32_e32 vcc, s63, v2
	v_cmp_le_i32_e64 s[6:7], s65, v2
	s_cselect_b64 s[0:1], -1, 0
	v_cndmask_b32_e64 v3, 0, 1, vcc
	v_cndmask_b32_e64 v5, 0, 1, s[6:7]
	v_cmp_le_i32_e64 s[6:7], s64, v2
	s_add_i32 s10, s66, 0x80
	v_cmp_gt_i32_e64 s[4:5], s67, v2
	v_addc_co_u32_e64 v3, s[6:7], v5, v3, s[6:7]
	v_cndmask_b32_e32 v5, 0, v4, vcc
	v_cmp_gt_i32_e32 vcc, s65, v2
	v_lshlrev_b32_e32 v199, 24, v3
	v_mov_b32_e32 v50, 0
	v_cndmask_b32_e32 v5, v6, v5, vcc
	v_cmp_gt_i32_e32 vcc, s64, v2
	s_mov_b32 s72, 0
	s_movk_i32 s73, 0x80
	v_cndmask_b32_e32 v5, v7, v5, vcc
	v_sub_u32_e32 v198, v2, v5
	v_add_u32_e32 v2, s10, v1
	v_cmp_le_i32_e32 vcc, s63, v2
	v_cmp_le_i32_e64 s[8:9], s65, v2
	v_cmp_gt_i32_e64 s[6:7], s67, v2
	v_cndmask_b32_e64 v3, 0, 1, vcc
	v_cndmask_b32_e64 v5, 0, 1, s[8:9]
	v_cmp_le_i32_e64 s[8:9], s64, v2
	v_mov_b32_e32 v51, v50
	v_mov_b32_e32 v52, v50
	v_addc_co_u32_e64 v3, s[8:9], v5, v3, s[8:9]
	v_cndmask_b32_e32 v5, 0, v4, vcc
	v_cmp_gt_i32_e32 vcc, s65, v2
	v_lshlrev_b32_e32 v201, 24, v3
	v_mov_b32_e32 v53, v50
	v_cndmask_b32_e32 v5, v6, v5, vcc
	v_cmp_gt_i32_e32 vcc, s64, v2
	v_mov_b32_e32 v58, v50
	v_mov_b32_e32 v59, v50
	v_cndmask_b32_e32 v5, v7, v5, vcc
	v_sub_u32_e32 v200, v2, v5
	v_add_u32_e32 v2, s10, v178
	v_cmp_le_i32_e32 vcc, s63, v2
	v_cmp_le_i32_e64 s[10:11], s65, v2
	v_cmp_gt_i32_e64 s[8:9], s67, v2
	v_cndmask_b32_e64 v3, 0, 1, vcc
	v_cndmask_b32_e32 v4, 0, v4, vcc
	v_cmp_gt_i32_e32 vcc, s65, v2
	v_cndmask_b32_e64 v5, 0, 1, s[10:11]
	v_cmp_le_i32_e64 s[10:11], s64, v2
	v_cndmask_b32_e32 v4, v6, v4, vcc
	v_cmp_gt_i32_e32 vcc, s64, v2
	v_addc_co_u32_e64 v3, s[10:11], v5, v3, s[10:11]
	s_nop 0
	v_cndmask_b32_e32 v4, v7, v4, vcc
	v_sub_u32_e32 v202, v2, v4
	v_lshlrev_b32_e32 v203, 24, v3
	s_nop 1
	v_mov_b64_e32 v[54:55], 0
	v_mov_b64_e32 v[56:57], 0
	v_mov_b64_e32 v[60:61], 0
	v_mov_b64_e32 v[62:63], 0
	v_mov_b64_e32 v[64:65], 0
	v_mov_b64_e32 v[66:67], 0
	v_mov_b64_e32 v[68:69], 0
	v_mov_b64_e32 v[70:71], 0
	v_mov_b64_e32 v[72:73], 0
	v_mov_b64_e32 v[74:75], 0
	v_mov_b64_e32 v[76:77], 0
	v_mov_b64_e32 v[78:79], 0
	v_mov_b64_e32 v[80:81], 0
	v_mov_b64_e32 v[82:83], 0
	v_mov_b64_e32 v[84:85], 0
	v_mov_b64_e32 v[86:87], 0
	v_mov_b64_e32 v[88:89], 0
	v_mov_b64_e32 v[90:91], 0
	v_mov_b64_e32 v[92:93], 0
	v_mov_b64_e32 v[94:95], 0
	v_mov_b64_e32 v[96:97], 0
	v_mov_b64_e32 v[98:99], 0
	v_mov_b64_e32 v[100:101], 0
	v_mov_b64_e32 v[102:103], 0
	v_mov_b64_e32 v[104:105], 0
	v_mov_b64_e32 v[106:107], 0
	v_mov_b64_e32 v[108:109], 0
	v_mov_b64_e32 v[110:111], 0
	v_mov_b64_e32 v[112:113], 0
	v_mov_b64_e32 v[114:115], 0
	v_mov_b64_e32 v[116:117], 0
	v_mov_b64_e32 v[118:119], 0
	v_mov_b64_e32 v[120:121], 0
	v_mov_b64_e32 v[122:123], 0
	v_mov_b64_e32 v[124:125], 0
	v_mov_b64_e32 v[126:127], 0
	v_mov_b64_e32 v[128:129], 0
	v_mov_b64_e32 v[130:131], 0
	v_mov_b64_e32 v[132:133], 0
	v_mov_b64_e32 v[134:135], 0
	v_mov_b64_e32 v[136:137], 0
	v_mov_b64_e32 v[138:139], 0
	v_mov_b64_e32 v[140:141], 0
	v_mov_b64_e32 v[142:143], 0
	v_mov_b64_e32 v[144:145], 0
	v_mov_b64_e32 v[146:147], 0
	v_mov_b64_e32 v[148:149], 0
	v_mov_b64_e32 v[150:151], 0
	v_mov_b64_e32 v[152:153], 0
	v_mov_b64_e32 v[154:155], 0
	v_mov_b64_e32 v[156:157], 0
	v_mov_b64_e32 v[158:159], 0
	v_mov_b64_e32 v[160:161], 0
	v_mov_b64_e32 v[162:163], 0
	v_mov_b64_e32 v[164:165], 0
	v_mov_b64_e32 v[166:167], 0
	v_mov_b64_e32 v[168:169], 0
	v_mov_b64_e32 v[170:171], 0
	v_mov_b64_e32 v[172:173], 0
	v_mov_b64_e32 v[174:175], 0
	v_mov_b64_e32 v[176:177], 0


	s_branch .LBB0_1841

.LBB0_1862:
	v_cmp_lt_i64_e64 s[4:5], s[4:5], v[130:131]
	s_lshl_b32 s53, s29, 17
	s_lshl_b32 s54, s28, 17
	s_and_b64 vcc, exec, s[0:1]
	v_mov_b32_e32 v125, 0
	s_cbranch_vccnz .LBB0_1854
	s_and_b64 s[4:5], s[4:5], exec
	v_mov_b32_e32 v2, 0
	s_cselect_b32 s4, s53, s55
	s_cselect_b32 s5, s54, s56
	s_addk_i32 s55, 0x80
	s_addk_i32 s56, 0x100
	s_mov_b32 s57, 0
	s_nop 1
	v_mov_b32_e32 v3, 0
	v_mov_b64_e32 v[4:5], 0
	v_mov_b64_e32 v[6:7], 0
	v_mov_b64_e32 v[8:9], 0
	v_mov_b64_e32 v[10:11], 0
	v_mov_b64_e32 v[12:13], 0
	v_mov_b64_e32 v[14:15], 0
	v_mov_b64_e32 v[16:17], 0
	v_mov_b64_e32 v[18:19], 0
	v_mov_b64_e32 v[20:21], 0
	v_mov_b64_e32 v[22:23], 0
	v_mov_b64_e32 v[24:25], 0
	v_mov_b64_e32 v[26:27], 0
	v_mov_b64_e32 v[28:29], 0
	v_mov_b64_e32 v[30:31], 0
	v_mov_b64_e32 v[32:33], 0
	v_mov_b64_e32 v[34:35], 0
	v_mov_b64_e32 v[36:37], 0
	v_mov_b64_e32 v[38:39], 0
	v_mov_b64_e32 v[40:41], 0
	v_mov_b64_e32 v[42:43], 0
	v_mov_b64_e32 v[44:45], 0
	v_mov_b64_e32 v[46:47], 0
	v_mov_b64_e32 v[48:49], 0
	v_mov_b64_e32 v[50:51], 0
	v_mov_b64_e32 v[52:53], 0
	v_mov_b64_e32 v[54:55], 0
	v_mov_b64_e32 v[56:57], 0
	v_mov_b64_e32 v[58:59], 0
	v_mov_b64_e32 v[60:61], 0
	v_mov_b64_e32 v[62:63], 0
	v_mov_b64_e32 v[64:65], 0
	v_mov_b64_e32 v[66:67], 0
	v_mov_b64_e32 v[68:69], 0
	v_mov_b64_e32 v[70:71], 0
	v_mov_b64_e32 v[72:73], 0
	v_mov_b64_e32 v[74:75], 0
	v_mov_b64_e32 v[76:77], 0
	v_mov_b64_e32 v[78:79], 0
	v_mov_b64_e32 v[80:81], 0
	v_mov_b64_e32 v[82:83], 0
	v_mov_b64_e32 v[84:85], 0
	v_mov_b64_e32 v[86:87], 0
	v_mov_b64_e32 v[88:89], 0
	v_mov_b64_e32 v[90:91], 0
	v_mov_b64_e32 v[92:93], 0
	v_mov_b64_e32 v[94:95], 0
	v_mov_b64_e32 v[96:97], 0
	v_mov_b64_e32 v[98:99], 0
	v_mov_b64_e32 v[100:101], 0
	v_mov_b64_e32 v[102:103], 0
	v_mov_b64_e32 v[104:105], 0
	v_mov_b64_e32 v[106:107], 0
	v_mov_b64_e32 v[108:109], 0
	v_mov_b64_e32 v[110:111], 0
	v_mov_b64_e32 v[112:113], 0
	v_mov_b64_e32 v[114:115], 0
	v_mov_b64_e32 v[116:117], 0
	v_mov_b64_e32 v[118:119], 0
	v_mov_b64_e32 v[120:121], 0
	v_mov_b64_e32 v[122:123], 0
	v_mov_b64_e32 v[124:125], 0
	v_mov_b64_e32 v[126:127], 0
	v_mov_b64_e32 v[128:129], 0



.LBB0_1945:
	s_lshl_b32 s44, s41, 17
	s_lshl_b32 s15, s40, 20
	s_lshl_b32 s43, s42, 9
	s_add_i32 s44, s44, s15
	s_andn2_b64 vcc, exec, s[6:7]
	v_mov_b32_e32 v125, 0
	s_cbranch_vccnz .LBB0_1936
	s_and_b64 s[16:17], s[10:11], exec
	s_cselect_b32 s46, s43, s48
	s_cselect_b32 s47, s44, s49
	s_ashr_i32 s15, s14, 31
	s_lshl_b64 s[14:15], s[14:15], 11
	s_add_u32 s14, s30, s14
	v_mov_b32_e32 v2, 0
	s_addc_u32 s15, s31, s15
	s_addk_i32 s48, 0x80
	s_addk_i32 s49, 0x100
	s_mov_b32 s50, 0
	s_nop 1
	v_mov_b32_e32 v3, 0
	v_mov_b64_e32 v[4:5], 0
	v_mov_b64_e32 v[6:7], 0
	v_mov_b64_e32 v[8:9], 0
	v_mov_b64_e32 v[10:11], 0
	v_mov_b64_e32 v[12:13], 0
	v_mov_b64_e32 v[14:15], 0
	v_mov_b64_e32 v[16:17], 0
	v_mov_b64_e32 v[18:19], 0
	v_mov_b64_e32 v[20:21], 0
	v_mov_b64_e32 v[22:23], 0
	v_mov_b64_e32 v[24:25], 0
	v_mov_b64_e32 v[26:27], 0
	v_mov_b64_e32 v[28:29], 0
	v_mov_b64_e32 v[30:31], 0
	v_mov_b64_e32 v[32:33], 0
	v_mov_b64_e32 v[34:35], 0
	v_mov_b64_e32 v[36:37], 0
	v_mov_b64_e32 v[38:39], 0
	v_mov_b64_e32 v[40:41], 0
	v_mov_b64_e32 v[42:43], 0
	v_mov_b64_e32 v[44:45], 0
	v_mov_b64_e32 v[46:47], 0
	v_mov_b64_e32 v[48:49], 0
	v_mov_b64_e32 v[50:51], 0
	v_mov_b64_e32 v[52:53], 0
	v_mov_b64_e32 v[54:55], 0
	v_mov_b64_e32 v[56:57], 0
	v_mov_b64_e32 v[58:59], 0
	v_mov_b64_e32 v[60:61], 0
	v_mov_b64_e32 v[62:63], 0
	v_mov_b64_e32 v[64:65], 0
	v_mov_b64_e32 v[70:71], 0
	v_mov_b64_e32 v[72:73], 0
	v_mov_b64_e32 v[74:75], 0
	v_mov_b64_e32 v[76:77], 0
	v_mov_b64_e32 v[78:79], 0
	v_mov_b64_e32 v[80:81], 0
	v_mov_b64_e32 v[82:83], 0
	v_mov_b64_e32 v[84:85], 0
	v_mov_b64_e32 v[86:87], 0
	v_mov_b64_e32 v[88:89], 0
	v_mov_b64_e32 v[90:91], 0
	v_mov_b64_e32 v[92:93], 0
	v_mov_b64_e32 v[94:95], 0
	v_mov_b64_e32 v[96:97], 0
	v_mov_b64_e32 v[98:99], 0
	v_mov_b64_e32 v[100:101], 0
	v_mov_b64_e32 v[102:103], 0
	v_mov_b64_e32 v[104:105], 0
	v_mov_b64_e32 v[106:107], 0
	v_mov_b64_e32 v[108:109], 0
	v_mov_b64_e32 v[110:111], 0
	v_mov_b64_e32 v[112:113], 0
	v_mov_b64_e32 v[114:115], 0
	v_mov_b64_e32 v[116:117], 0
	v_mov_b64_e32 v[118:119], 0
	v_mov_b64_e32 v[120:121], 0
	v_mov_b64_e32 v[122:123], 0
	v_mov_b64_e32 v[124:125], 0
	v_mov_b64_e32 v[126:127], 0
	v_mov_b64_e32 v[128:129], 0
	v_mov_b64_e32 v[228:229], 0
	v_mov_b64_e32 v[230:231], 0


	s_branch .LBB0_1948

.LBB0_2283:
	s_lshl_b32 s45, s41, 17
	s_lshl_b32 s15, s40, 20
	s_lshl_b32 s43, s42, 9
	s_add_i32 s45, s45, s15
	s_andn2_b64 vcc, exec, s[6:7]
	v_mov_b32_e32 v125, 0
	s_cbranch_vccnz .LBB0_2274
	s_and_b64 s[16:17], s[10:11], exec
	s_cselect_b32 s46, s43, s48
	s_cselect_b32 s47, s45, s49
	s_ashr_i32 s15, s14, 31
	s_lshl_b64 s[14:15], s[14:15], 11
	s_add_u32 s14, s30, s14
	v_mov_b32_e32 v2, 0
	s_addc_u32 s15, s31, s15
	s_addk_i32 s48, 0x80
	s_addk_i32 s49, 0x100
	s_mov_b32 s50, 0
	s_nop 1
	v_mov_b32_e32 v3, 0
	v_mov_b64_e32 v[4:5], 0
	v_mov_b64_e32 v[6:7], 0
	v_mov_b64_e32 v[8:9], 0
	v_mov_b64_e32 v[10:11], 0
	v_mov_b64_e32 v[12:13], 0
	v_mov_b64_e32 v[14:15], 0
	v_mov_b64_e32 v[16:17], 0
	v_mov_b64_e32 v[18:19], 0
	v_mov_b64_e32 v[20:21], 0
	v_mov_b64_e32 v[22:23], 0
	v_mov_b64_e32 v[24:25], 0
	v_mov_b64_e32 v[26:27], 0
	v_mov_b64_e32 v[28:29], 0
	v_mov_b64_e32 v[30:31], 0
	v_mov_b64_e32 v[32:33], 0
	v_mov_b64_e32 v[34:35], 0
	v_mov_b64_e32 v[36:37], 0
	v_mov_b64_e32 v[38:39], 0
	v_mov_b64_e32 v[40:41], 0
	v_mov_b64_e32 v[42:43], 0
	v_mov_b64_e32 v[44:45], 0
	v_mov_b64_e32 v[46:47], 0
	v_mov_b64_e32 v[48:49], 0
	v_mov_b64_e32 v[50:51], 0
	v_mov_b64_e32 v[52:53], 0
	v_mov_b64_e32 v[54:55], 0
	v_mov_b64_e32 v[56:57], 0
	v_mov_b64_e32 v[58:59], 0
	v_mov_b64_e32 v[60:61], 0
	v_mov_b64_e32 v[62:63], 0
	v_mov_b64_e32 v[64:65], 0
	v_mov_b64_e32 v[70:71], 0
	v_mov_b64_e32 v[72:73], 0
	v_mov_b64_e32 v[74:75], 0
	v_mov_b64_e32 v[76:77], 0
	v_mov_b64_e32 v[78:79], 0
	v_mov_b64_e32 v[80:81], 0
	v_mov_b64_e32 v[82:83], 0
	v_mov_b64_e32 v[84:85], 0
	v_mov_b64_e32 v[86:87], 0
	v_mov_b64_e32 v[88:89], 0
	v_mov_b64_e32 v[90:91], 0
	v_mov_b64_e32 v[92:93], 0
	v_mov_b64_e32 v[94:95], 0
	v_mov_b64_e32 v[96:97], 0
	v_mov_b64_e32 v[98:99], 0
	v_mov_b64_e32 v[100:101], 0
	v_mov_b64_e32 v[102:103], 0
	v_mov_b64_e32 v[104:105], 0
	v_mov_b64_e32 v[106:107], 0
	v_mov_b64_e32 v[108:109], 0
	v_mov_b64_e32 v[110:111], 0
	v_mov_b64_e32 v[112:113], 0
	v_mov_b64_e32 v[114:115], 0
	v_mov_b64_e32 v[116:117], 0
	v_mov_b64_e32 v[118:119], 0
	v_mov_b64_e32 v[120:121], 0
	v_mov_b64_e32 v[122:123], 0
	v_mov_b64_e32 v[124:125], 0
	v_mov_b64_e32 v[126:127], 0
	v_mov_b64_e32 v[128:129], 0
	v_mov_b64_e32 v[228:229], 0
	v_mov_b64_e32 v[230:231], 0


	s_branch .LBB0_2286

.LBB0_2396:
	s_lshl_b32 s53, s52, 19
	s_lshl_b32 s54, s51, 19
	s_and_b64 vcc, exec, s[0:1]
	v_mov_b32_e32 v137, 0
	s_cbranch_vccnz .LBB0_2392
	v_cmp_lt_i64_e32 vcc, s[34:35], v[166:167]
	s_and_b64 s[34:35], vcc, exec
	v_mov_b32_e32 v2, 0
	s_cselect_b32 s34, s53, s56
	s_cselect_b32 s35, s54, s57
	s_addk_i32 s56, 0x80
	s_addk_i32 s57, 0x100
	s_mov_b32 s58, 0
	s_nop 1
	v_mov_b32_e32 v3, 0
	v_mov_b64_e32 v[4:5], 0
	v_mov_b64_e32 v[6:7], 0
	v_mov_b64_e32 v[8:9], 0
	v_mov_b64_e32 v[10:11], 0
	v_mov_b64_e32 v[12:13], 0
	v_mov_b64_e32 v[14:15], 0
	v_mov_b64_e32 v[16:17], 0
	v_mov_b64_e32 v[18:19], 0
	v_mov_b64_e32 v[20:21], 0
	v_mov_b64_e32 v[22:23], 0
	v_mov_b64_e32 v[24:25], 0
	v_mov_b64_e32 v[26:27], 0
	v_mov_b64_e32 v[28:29], 0
	v_mov_b64_e32 v[30:31], 0
	v_mov_b64_e32 v[32:33], 0
	v_mov_b64_e32 v[34:35], 0
	v_mov_b64_e32 v[36:37], 0
	v_mov_b64_e32 v[38:39], 0
	v_mov_b64_e32 v[40:41], 0
	v_mov_b64_e32 v[42:43], 0
	v_mov_b64_e32 v[44:45], 0
	v_mov_b64_e32 v[46:47], 0
	v_mov_b64_e32 v[48:49], 0
	v_mov_b64_e32 v[50:51], 0
	v_mov_b64_e32 v[52:53], 0
	v_mov_b64_e32 v[54:55], 0
	v_mov_b64_e32 v[56:57], 0
	v_mov_b64_e32 v[58:59], 0
	v_mov_b64_e32 v[60:61], 0
	v_mov_b64_e32 v[62:63], 0
	v_mov_b64_e32 v[64:65], 0
	v_mov_b64_e32 v[66:67], 0
	v_mov_b64_e32 v[68:69], 0
	v_mov_b64_e32 v[70:71], 0
	v_mov_b64_e32 v[72:73], 0
	v_mov_b64_e32 v[74:75], 0
	v_mov_b64_e32 v[76:77], 0
	v_mov_b64_e32 v[78:79], 0
	v_mov_b64_e32 v[80:81], 0
	v_mov_b64_e32 v[82:83], 0
	v_mov_b64_e32 v[84:85], 0
	v_mov_b64_e32 v[86:87], 0
	v_mov_b64_e32 v[88:89], 0
	v_mov_b64_e32 v[90:91], 0
	v_mov_b64_e32 v[92:93], 0
	v_mov_b64_e32 v[94:95], 0
	v_mov_b64_e32 v[96:97], 0
	v_mov_b64_e32 v[106:107], 0
	v_mov_b64_e32 v[108:109], 0
	v_mov_b64_e32 v[110:111], 0
	v_mov_b64_e32 v[112:113], 0
	v_mov_b64_e32 v[114:115], 0
	v_mov_b64_e32 v[116:117], 0
	v_mov_b64_e32 v[118:119], 0
	v_mov_b64_e32 v[120:121], 0
	v_mov_b64_e32 v[122:123], 0
	v_mov_b64_e32 v[124:125], 0
	v_mov_b64_e32 v[126:127], 0
	v_mov_b64_e32 v[128:129], 0
	v_mov_b64_e32 v[130:131], 0
	v_mov_b64_e32 v[132:133], 0
	v_mov_b64_e32 v[134:135], 0
	v_mov_b64_e32 v[136:137], 0



.LBB0_2503:
	v_cmp_lt_i64_e64 s[2:3], s[2:3], v[166:167]
	s_lshl_b32 s52, s37, 19
	s_lshl_b32 s53, s36, 19
	s_andn2_b64 vcc, exec, s[18:19]
	v_mov_b32_e32 v137, 0
	s_cbranch_vccnz .LBB0_2495
	s_and_b64 s[2:3], s[2:3], exec
	v_mov_b32_e32 v2, 0
	s_cselect_b32 s2, s52, s55
	s_cselect_b32 s3, s53, s56
	s_addk_i32 s55, 0x80
	s_addk_i32 s56, 0x100
	s_mov_b32 s57, 0
	s_nop 1
	v_mov_b32_e32 v3, 0
	v_mov_b64_e32 v[4:5], 0
	v_mov_b64_e32 v[6:7], 0
	v_mov_b64_e32 v[8:9], 0
	v_mov_b64_e32 v[10:11], 0
	v_mov_b64_e32 v[12:13], 0
	v_mov_b64_e32 v[14:15], 0
	v_mov_b64_e32 v[16:17], 0
	v_mov_b64_e32 v[18:19], 0
	v_mov_b64_e32 v[20:21], 0
	v_mov_b64_e32 v[22:23], 0
	v_mov_b64_e32 v[24:25], 0
	v_mov_b64_e32 v[26:27], 0
	v_mov_b64_e32 v[28:29], 0
	v_mov_b64_e32 v[30:31], 0
	v_mov_b64_e32 v[32:33], 0
	v_mov_b64_e32 v[34:35], 0
	v_mov_b64_e32 v[36:37], 0
	v_mov_b64_e32 v[38:39], 0
	v_mov_b64_e32 v[40:41], 0
	v_mov_b64_e32 v[42:43], 0
	v_mov_b64_e32 v[44:45], 0
	v_mov_b64_e32 v[46:47], 0
	v_mov_b64_e32 v[48:49], 0
	v_mov_b64_e32 v[50:51], 0
	v_mov_b64_e32 v[52:53], 0
	v_mov_b64_e32 v[54:55], 0
	v_mov_b64_e32 v[56:57], 0
	v_mov_b64_e32 v[58:59], 0
	v_mov_b64_e32 v[60:61], 0
	v_mov_b64_e32 v[62:63], 0
	v_mov_b64_e32 v[64:65], 0
	v_mov_b64_e32 v[66:67], 0
	v_mov_b64_e32 v[68:69], 0
	v_mov_b64_e32 v[70:71], 0
	v_mov_b64_e32 v[72:73], 0
	v_mov_b64_e32 v[74:75], 0
	v_mov_b64_e32 v[76:77], 0
	v_mov_b64_e32 v[78:79], 0
	v_mov_b64_e32 v[80:81], 0
	v_mov_b64_e32 v[82:83], 0
	v_mov_b64_e32 v[84:85], 0
	v_mov_b64_e32 v[86:87], 0
	v_mov_b64_e32 v[88:89], 0
	v_mov_b64_e32 v[90:91], 0
	v_mov_b64_e32 v[92:93], 0
	v_mov_b64_e32 v[94:95], 0
	v_mov_b64_e32 v[96:97], 0
	v_mov_b64_e32 v[106:107], 0
	v_mov_b64_e32 v[108:109], 0
	v_mov_b64_e32 v[110:111], 0
	v_mov_b64_e32 v[112:113], 0
	v_mov_b64_e32 v[114:115], 0
	v_mov_b64_e32 v[116:117], 0
	v_mov_b64_e32 v[118:119], 0
	v_mov_b64_e32 v[120:121], 0
	v_mov_b64_e32 v[122:123], 0
	v_mov_b64_e32 v[124:125], 0
	v_mov_b64_e32 v[126:127], 0
	v_mov_b64_e32 v[128:129], 0
	v_mov_b64_e32 v[130:131], 0
	v_mov_b64_e32 v[132:133], 0
	v_mov_b64_e32 v[134:135], 0
	v_mov_b64_e32 v[136:137], 0


